# s18
# baseline (speedup 1.0000x reference)
_Z11attn_kernelILi4EEvPKfS1_S1_S1_S1_S1_PKcPf:
	s_load_dwordx2 s[24:25], s[0:1], 0x30
	s_load_dwordx8 s[8:15], s[0:1], 0x0
	s_load_dwordx4 s[16:19], s[0:1], 0x20
	v_lshrrev_b32_e32 v63, 6, v0
	v_and_b32_e32 v57, 15, v0
	v_bfe_u32 v1, v0, 4, 2
	v_lshrrev_b32_e32 v2, 2, v57
	v_mul_u32_u24_e32 v4, 3, v1
	v_mul_u32_u24_e32 v2, 3, v2
	v_mad_u32_u24 v4, v63, 12, v4
	v_mad_u32_u24 v2, v63, 12, v2
	v_lshlrev_b32_e32 v4, 2, v4
	v_lshlrev_b32_e32 v2, 2, v2
	v_and_b32_e32 v104, 63, v0
	v_lshlrev_b32_e32 v60, 5, v57
	v_lshlrev_b32_e32 v58, 3, v1
	v_add_u32_e32 v3, v60, v58
	v_lshrrev_b32_e32 v56, 4, v0
	v_lshlrev_b32_e32 v54, 4, v57
	v_mov_b32_e32 v59, 0
	s_movk_i32 s4, 0xe0
	v_cmp_gt_u32_e64 s[4:5], s4, v0
	s_lshl_b32 s26, s2, 8
	s_lshl_b32 s27, s2, 9
	s_mul_i32 s28, s2, 14
	s_add_u32 s26, s26, 0x164000
	s_add_u32 s27, s27, 0x80000
	s_add_u32 s20, s26, 0xc0
	v_lshlrev_b32_e32 v5, 2, v57
	v_lshlrev_b32_e32 v147, 6, v57
	v_add_u32_e32 v2, s26, v2
	v_add_u32_e32 v4, s26, v4
	v_add_u32_e32 v3, s27, v3
	v_mul_u32_u24_e32 v156, 0x140, v1
	s_movk_i32 s21, 0x500
	v_mad_u32_u24 v156, v63, s21, v156
	v_lshl_or_b32 v156, v57, 2, v156
	v_add_u32_e32 v156, 0x1c00, v156
	v_lshlrev_b32_e32 v157, 5, v56
	v_cmp_gt_u32_e32 vcc, 3, v57
	v_add_u32_e32 v158, 4, v57
	v_lshlrev_b32_e32 v159, 2, v57
	s_movk_i32 s21, 0x50
	v_cndmask_b32_e32 v158, 4, v158, vcc
	v_mad_u32_u24 v159, v56, s21, v159
	v_lshl_add_u32 v158, v158, 2, v157
	v_mul_u32_u24_e32 v250, 0x50, v56
	v_or_b32_e32 v250, 0x3800, v250
	v_lshl_add_u32 v251, v57, 1, v250
	v_mul_u32_u24_e32 v252, 0x50, v57
	v_lshl_add_u32 v252, v58, 1, v252
	v_lshlrev_b32_e32 v253, 2, v57
	v_and_b32_e32 v254, 0xc0, v0
	v_lshlrev_b32_e32 v255, 11, v1
	v_or3_b32 v253, v253, v254, v255
	v_add_u32_e32 v254, s28, v56
	v_lshl_add_u32 v254, v254, 9, v54
	v_lshl_or_b32 v255, v56, 9, v54
	s_waitcnt lgkmcnt(0)
	global_load_dwordx3 v[80:82], v2, s[24:25]
	global_load_dwordx3 v[84:86], v4, s[24:25]
	global_load_dwordx2 v[64:65], v3, s[24:25]
	s_load_dword s3, s[24:25], s20
	s_add_u32 s22, s24, 0x160000
	s_addc_u32 s23, s25, 0
	v_cndmask_b32_e64 v62, 13, v56, s[4:5]
	v_add_u32_e32 v3, s28, v62
	v_mad_u32_u24 v144, v3, 36, v5
	v_mad_u32_u24 v146, v3, 12, v5
	v_add_u32_e32 v145, -36, v146
	v_add_u32_e32 v146, -48, v146
	v_lshl_or_b32 v147, v63, 10, v147
	v_lshl_or_b32 v147, v1, 4, v147
	v_or_b32_e32 v148, 0x1000, v147
	v_lshlrev_b32_e32 v149, 4, v104
	v_lshlrev_b32_e32 v150, 9, v3
	v_add_u32_e32 v150, v150, v54
	v_and_b32_e32 v87, 3, v57
	v_lshlrev_b32_e32 v87, 4, v87
	v_lshl_or_b32 v87, v1, 6, v87
	v_lshlrev_b32_e32 v88, 3, v57
	s_add_u32 s26, s24, 0x100000
	s_addc_u32 s27, s25, 0
	s_add_u32 s28, s24, 0x140000
	s_addc_u32 s29, s25, 0
	s_movk_i32 s6, 0x140
	v_cmp_gt_u32_e32 vcc, s6, v0
	v_lshlrev_b32_e32 v22, 2, v0
	v_mov_b32_e32 v23, 0
	s_and_saveexec_b64 s[6:7], vcc
	ds_write_b32 v22, v23 offset:14336
	s_or_b64 exec, exec, s[6:7]
	v_cmp_gt_u32_e32 vcc, 64, v0
	s_and_saveexec_b64 s[6:7], vcc
	ds_write_b32 v22, v23 offset:15360
	s_or_b64 exec, exec, s[6:7]
	v_mov_b32_e32 v45, 0xc9c35000
	s_mov_b32 s30, 0x3db8aa3b
	s_mov_b32 s31, 0x3db8aa3b
	v_mov_b32_e32 v121, 0x3fb8aa3b
	v_mov_b32_e32 v35, 0
	v_mov_b32_e32 v44, v45
	s_waitcnt lgkmcnt(0)
	s_bitcmp0_b32 s3, 1
	s_cselect_b64 s[20:21], -1, 0
	s_cbranch_scc1 .LBB1_16
	v_bfe_u32 v46, s3, v57, 1
	v_cmp_eq_u32_e32 vcc, 0, v46
	s_nop 1
	v_cndmask_b32_e32 v47, 0, v45, vcc
	v_cndmask_b32_e64 v55, 1.0, 0, vcc
	s_nop 0
	v_mov_b32_dpp v34, v47 row_newbcast:0 row_mask:0xf bank_mask:0xf bound_ctrl:1
	v_mov_b32_dpp v36, v47 row_newbcast:2 row_mask:0xf bank_mask:0xf bound_ctrl:1
	v_mov_b32_dpp v37, v47 row_newbcast:3 row_mask:0xf bank_mask:0xf bound_ctrl:1
	v_mov_b32_dpp v22, v47 row_newbcast:4 row_mask:0xf bank_mask:0xf bound_ctrl:1
	v_mov_b32_dpp v23, v47 row_newbcast:5 row_mask:0xf bank_mask:0xf bound_ctrl:1
	v_mov_b32_dpp v24, v47 row_newbcast:6 row_mask:0xf bank_mask:0xf bound_ctrl:1
	v_mov_b32_dpp v25, v47 row_newbcast:7 row_mask:0xf bank_mask:0xf bound_ctrl:1
	v_mov_b32_dpp v38, v47 row_newbcast:8 row_mask:0xf bank_mask:0xf bound_ctrl:1
	v_mov_b32_dpp v39, v47 row_newbcast:9 row_mask:0xf bank_mask:0xf bound_ctrl:1
	v_mov_b32_dpp v40, v47 row_newbcast:10 row_mask:0xf bank_mask:0xf bound_ctrl:1
	v_mov_b32_dpp v41, v47 row_newbcast:11 row_mask:0xf bank_mask:0xf bound_ctrl:1
	v_mov_b32_dpp v42, v47 row_newbcast:12 row_mask:0xf bank_mask:0xf bound_ctrl:1
	v_mov_b32_dpp v43, v47 row_newbcast:13 row_mask:0xf bank_mask:0xf bound_ctrl:1
	s_waitcnt vmcnt(1)
	v_lshl_add_u32 v72, v80, 9, v87
	v_lshl_add_u32 v73, v81, 9, v87
	v_lshl_add_u32 v74, v82, 9, v87
	global_load_dwordx4 v[50:53], v72, s[24:25]
	global_load_dwordx4 v[46:49], v72, s[24:25] offset:256
	global_load_dwordx4 v[14:17], v73, s[24:25]
	global_load_dwordx4 v[10:13], v73, s[24:25] offset:256
	global_load_dwordx4 v[6:9], v74, s[24:25]
	global_load_dwordx4 v[2:5], v74, s[24:25] offset:256
	v_lshl_add_u32 v75, v84, 8, v54
	v_lshl_add_u32 v78, v84, 7, v88
	v_lshl_add_u32 v76, v85, 8, v54
	v_lshl_add_u32 v79, v85, 7, v88
	v_lshl_add_u32 v77, v86, 8, v54
	v_lshl_add_u32 v80, v86, 7, v88
	global_load_dwordx4 v[30:33], v75, s[26:27]
	global_load_dwordx2 v[70:71], v78, s[28:29]
	global_load_dwordx4 v[26:29], v76, s[26:27]
	global_load_dwordx2 v[66:67], v79, s[28:29]
	global_load_dwordx4 v[18:21], v77, s[26:27]
	global_load_dwordx2 v[68:69], v80, s[28:29]
	s_mov_b32 exec_lo, 0x1ff01ff
	s_mov_b32 exec_hi, 0x1ff01ff
	global_load_dword v120, v144, s[10:11]
	s_mov_b32 exec_lo, 0xe000e00
	s_mov_b32 exec_hi, 0xe000e00
	global_load_dword v120, v145, s[12:13]
	s_mov_b32 exec_lo, 0x70007000
	s_mov_b32 exec_hi, 0x70007000
	global_load_dword v120, v146, s[14:15]
	s_mov_b64 exec, -1
	global_load_dwordx4 v[124:127], v147, s[22:23]
	global_load_dwordx4 v[128:131], v148, s[22:23]
	s_mov_b32 exec_hi, 0
	global_load_dwordx4 v[132:135], v149, s[16:17]
	s_mov_b32 exec_hi, -1
	s_mov_b32 exec_lo, 0
	global_load_dwordx4 v[132:135], v149, s[18:19] offset:-512
	s_mov_b32 exec_lo, -1
	global_load_dwordx4 v[136:139], v150, s[8:9]
	global_load_dwordx4 v[140:143], v150, s[8:9] offset:256
	v_mov_b32_e32 v75, 0
	v_mov_b32_e32 v79, 0
	v_mov_b32_e32 v83, 0
	s_waitcnt vmcnt(20)
	v_mfma_f32_16x16x32_fp8_fp8 v[160:163], v[50:51], v[64:65], v[34:37]
	v_mfma_f32_16x16x32_fp8_fp8 v[164:167], v[52:53], v[64:65], v[22:25]
	s_waitcnt vmcnt(19)
	v_mfma_f32_16x16x32_fp8_fp8 v[168:171], v[46:47], v[64:65], v[38:41]
	v_mfma_f32_16x16x32_fp8_fp8 v[172:175], v[48:49], v[64:65], v[42:45]
	s_nop 3
	v_max3_f32 v86, v160, v161, v162
	v_max3_f32 v87, v163, v164, v165
	v_max3_f32 v88, v166, v167, v168
	v_max3_f32 v89, v169, v170, v171
	v_max3_f32 v86, v86, v172, v173
	v_max3_f32 v87, v87, v88, v89
	v_max_f32_e32 v96, v86, v87
	v_mul_f32_e32 v98, 0xbdb8aa3b, v96
	v_pk_fma_f32 v[208:209], v[160:161], s[30:31], v[98:99] op_sel_hi:[1,1,0]
	v_pk_fma_f32 v[210:211], v[162:163], s[30:31], v[98:99] op_sel_hi:[1,1,0]
	v_pk_fma_f32 v[212:213], v[164:165], s[30:31], v[98:99] op_sel_hi:[1,1,0]
	v_pk_fma_f32 v[214:215], v[166:167], s[30:31], v[98:99] op_sel_hi:[1,1,0]
	v_pk_fma_f32 v[216:217], v[168:169], s[30:31], v[98:99] op_sel_hi:[1,1,0]
	v_pk_fma_f32 v[218:219], v[170:171], s[30:31], v[98:99] op_sel_hi:[1,1,0]
	v_pk_fma_f32 v[220:221], v[172:173], s[30:31], v[98:99] op_sel_hi:[1,1,0]
	v_exp_f32_e32 v208, v208
	v_exp_f32_e32 v209, v209
	v_exp_f32_e32 v210, v210
	v_exp_f32_e32 v211, v211
	v_exp_f32_e32 v212, v212
	v_exp_f32_e32 v213, v213
	v_exp_f32_e32 v214, v214
	v_exp_f32_e32 v215, v215
	v_exp_f32_e32 v216, v216
	v_exp_f32_e32 v217, v217
	v_exp_f32_e32 v218, v218
	v_exp_f32_e32 v219, v219
	v_exp_f32_e32 v220, v220
	v_exp_f32_e32 v221, v221
	s_waitcnt vmcnt(18)
	v_mfma_f32_16x16x32_fp8_fp8 v[176:179], v[14:15], v[64:65], v[34:37]
	v_mfma_f32_16x16x32_fp8_fp8 v[180:183], v[16:17], v[64:65], v[22:25]
	s_waitcnt vmcnt(17)
	v_mfma_f32_16x16x32_fp8_fp8 v[184:187], v[10:11], v[64:65], v[38:41]
	v_mfma_f32_16x16x32_fp8_fp8 v[188:191], v[12:13], v[64:65], v[42:45]
	v_pk_add_f32 v[86:87], v[208:209], v[210:211]
	v_pk_add_f32 v[88:89], v[212:213], v[214:215]
	v_pk_add_f32 v[90:91], v[216:217], v[218:219]
	v_pk_mul_f32 v[92:93], v[208:209], v[160:161]
	v_pk_mul_f32 v[94:95], v[210:211], v[162:163]
	v_pk_add_f32 v[86:87], v[86:87], v[220:221]
	v_pk_add_f32 v[88:89], v[88:89], v[90:91]
	v_pk_fma_f32 v[92:93], v[212:213], v[164:165], v[92:93]
	v_pk_fma_f32 v[94:95], v[214:215], v[166:167], v[94:95]
	v_pk_add_f32 v[86:87], v[86:87], v[88:89]
	v_pk_fma_f32 v[92:93], v[216:217], v[168:169], v[92:93]
	v_pk_fma_f32 v[94:95], v[218:219], v[170:171], v[94:95]
	v_add_f32_e32 v86, v86, v87
	v_pk_fma_f32 v[92:93], v[220:221], v[172:173], v[92:93]
	v_rcp_f32_e32 v87, v86
	v_pk_add_f32 v[92:93], v[92:93], v[94:95]
	v_mul_f32_e32 v87, v55, v87
	v_add_f32_e32 v92, v92, v93
	v_mul_f32_e32 v107, v86, v87
	v_mul_f32_e32 v92, v92, v87
	v_mul_f32_e32 v100, 0x43800000, v87
	v_mul_f32_e32 v103, 0x3d800000, v92
	v_max3_f32 v86, v176, v177, v178
	v_max3_f32 v87, v179, v180, v181
	v_max3_f32 v88, v182, v183, v184
	v_max3_f32 v89, v185, v186, v187
	v_max3_f32 v86, v86, v188, v189
	v_max3_f32 v87, v87, v88, v89
	v_max_f32_e32 v96, v86, v87
	v_mul_f32_e32 v98, 0xbdb8aa3b, v96
	v_pk_fma_f32 v[222:223], v[176:177], s[30:31], v[98:99] op_sel_hi:[1,1,0]
	v_pk_fma_f32 v[224:225], v[178:179], s[30:31], v[98:99] op_sel_hi:[1,1,0]
	v_pk_fma_f32 v[226:227], v[180:181], s[30:31], v[98:99] op_sel_hi:[1,1,0]
	v_pk_fma_f32 v[228:229], v[182:183], s[30:31], v[98:99] op_sel_hi:[1,1,0]
	v_pk_fma_f32 v[230:231], v[184:185], s[30:31], v[98:99] op_sel_hi:[1,1,0]
	v_pk_fma_f32 v[232:233], v[186:187], s[30:31], v[98:99] op_sel_hi:[1,1,0]
	v_pk_fma_f32 v[234:235], v[188:189], s[30:31], v[98:99] op_sel_hi:[1,1,0]
	v_exp_f32_e32 v222, v222
	v_exp_f32_e32 v223, v223
	v_exp_f32_e32 v224, v224
	v_exp_f32_e32 v225, v225
	v_exp_f32_e32 v226, v226
	v_exp_f32_e32 v227, v227
	v_exp_f32_e32 v228, v228
	v_exp_f32_e32 v229, v229
	v_exp_f32_e32 v230, v230
	v_exp_f32_e32 v231, v231
	v_exp_f32_e32 v232, v232
	v_exp_f32_e32 v233, v233
	v_exp_f32_e32 v234, v234
	v_exp_f32_e32 v235, v235
	s_waitcnt vmcnt(16)
	v_mfma_f32_16x16x32_fp8_fp8 v[192:195], v[6:7], v[64:65], v[34:37]
	v_mfma_f32_16x16x32_fp8_fp8 v[196:199], v[8:9], v[64:65], v[22:25]
	s_waitcnt vmcnt(15)
	v_mfma_f32_16x16x32_fp8_fp8 v[200:203], v[2:3], v[64:65], v[38:41]
	v_mfma_f32_16x16x32_fp8_fp8 v[204:207], v[4:5], v[64:65], v[42:45]
	v_pk_add_f32 v[86:87], v[222:223], v[224:225]
	v_pk_add_f32 v[88:89], v[226:227], v[228:229]
	v_pk_add_f32 v[90:91], v[230:231], v[232:233]
	v_pk_mul_f32 v[92:93], v[222:223], v[176:177]
	v_pk_mul_f32 v[94:95], v[224:225], v[178:179]
	v_pk_add_f32 v[86:87], v[86:87], v[234:235]
	v_pk_add_f32 v[88:89], v[88:89], v[90:91]
	v_pk_fma_f32 v[92:93], v[226:227], v[180:181], v[92:93]
	v_pk_fma_f32 v[94:95], v[228:229], v[182:183], v[94:95]
	v_pk_add_f32 v[86:87], v[86:87], v[88:89]
	v_pk_fma_f32 v[92:93], v[230:231], v[184:185], v[92:93]
	v_pk_fma_f32 v[94:95], v[232:233], v[186:187], v[94:95]
	v_add_f32_e32 v86, v86, v87
	v_pk_fma_f32 v[92:93], v[234:235], v[188:189], v[92:93]
	v_rcp_f32_e32 v87, v86
	v_pk_add_f32 v[92:93], v[92:93], v[94:95]
	v_mul_f32_e32 v87, v55, v87
	v_add_f32_e32 v92, v92, v93
	v_mul_f32_e32 v108, v86, v87
	v_mul_f32_e32 v92, v92, v87
	v_mul_f32_e32 v101, 0x43800000, v87
	v_mul_f32_e32 v105, 0x3d800000, v92
	v_max3_f32 v86, v192, v193, v194
	v_max3_f32 v87, v195, v196, v197
	v_max3_f32 v88, v198, v199, v200
	v_max3_f32 v89, v201, v202, v203
	v_max3_f32 v86, v86, v204, v205
	v_max3_f32 v87, v87, v88, v89
	v_max_f32_e32 v96, v86, v87
	v_mul_f32_e32 v98, 0xbdb8aa3b, v96
	v_pk_fma_f32 v[236:237], v[192:193], s[30:31], v[98:99] op_sel_hi:[1,1,0]
	v_pk_fma_f32 v[238:239], v[194:195], s[30:31], v[98:99] op_sel_hi:[1,1,0]
	v_pk_fma_f32 v[240:241], v[196:197], s[30:31], v[98:99] op_sel_hi:[1,1,0]
	v_pk_fma_f32 v[242:243], v[198:199], s[30:31], v[98:99] op_sel_hi:[1,1,0]
	v_pk_fma_f32 v[244:245], v[200:201], s[30:31], v[98:99] op_sel_hi:[1,1,0]
	v_pk_fma_f32 v[246:247], v[202:203], s[30:31], v[98:99] op_sel_hi:[1,1,0]
	v_pk_fma_f32 v[248:249], v[204:205], s[30:31], v[98:99] op_sel_hi:[1,1,0]
	v_exp_f32_e32 v236, v236
	v_exp_f32_e32 v237, v237
	v_exp_f32_e32 v238, v238
	v_exp_f32_e32 v239, v239
	v_exp_f32_e32 v240, v240
	v_exp_f32_e32 v241, v241
	v_exp_f32_e32 v242, v242
	v_exp_f32_e32 v243, v243
	v_exp_f32_e32 v244, v244
	v_exp_f32_e32 v245, v245
	v_exp_f32_e32 v246, v246
	v_exp_f32_e32 v247, v247
	v_exp_f32_e32 v248, v248
	v_exp_f32_e32 v249, v249
	v_pk_add_f32 v[86:87], v[236:237], v[238:239]
	v_pk_add_f32 v[88:89], v[240:241], v[242:243]
	v_pk_add_f32 v[90:91], v[244:245], v[246:247]
	v_pk_mul_f32 v[92:93], v[236:237], v[192:193]
	v_pk_mul_f32 v[94:95], v[238:239], v[194:195]
	v_pk_add_f32 v[86:87], v[86:87], v[248:249]
	v_pk_add_f32 v[88:89], v[88:89], v[90:91]
	v_pk_fma_f32 v[92:93], v[240:241], v[196:197], v[92:93]
	v_pk_fma_f32 v[94:95], v[242:243], v[198:199], v[94:95]
	v_pk_add_f32 v[86:87], v[86:87], v[88:89]
	v_pk_fma_f32 v[92:93], v[244:245], v[200:201], v[92:93]
	v_pk_fma_f32 v[94:95], v[246:247], v[202:203], v[94:95]
	v_add_f32_e32 v86, v86, v87
	v_pk_fma_f32 v[92:93], v[248:249], v[204:205], v[92:93]
	v_rcp_f32_e32 v87, v86
	v_pk_add_f32 v[92:93], v[92:93], v[94:95]
	v_mul_f32_e32 v87, v55, v87
	v_add_f32_e32 v92, v92, v93
	v_mul_f32_e32 v109, v86, v87
	v_mul_f32_e32 v92, v92, v87
	v_mul_f32_e32 v102, 0x43800000, v87
	v_mul_f32_e32 v106, 0x3d800000, v92
	v_max3_f32 v122, v103, v105, v106
	v_cmp_gt_u32_e64 s[6:7], 16, v104
	v_mov_b32_e32 v123, v122
	s_nop 1
	v_permlane16_swap_b32_e32 v122, v123
	v_max_f32_e32 v122, v122, v123
	v_mov_b32_e32 v123, v122
	s_nop 1
	v_permlane32_swap_b32_e32 v122, v123
	v_max_f32_e32 v36, v122, v123
	v_mul_f32_e32 v123, 0x3fb8aa3b, v36
	v_fma_f32 v111, v103, v121, -v123
	v_exp_f32_e32 v111, v111
	s_nop 0
	v_mul_f32_e32 v112, v111, v100
	v_mul_f32_e32 v110, v111, v107
	v_mov_b32_e32 v114, v111
	v_pk_mul_f32 v[208:209], v[208:209], v[112:113] op_sel_hi:[1,0]
	v_pk_mul_f32 v[210:211], v[210:211], v[112:113] op_sel_hi:[1,0]
	v_pk_mul_f32 v[212:213], v[212:213], v[112:113] op_sel_hi:[1,0]
	v_pk_mul_f32 v[214:215], v[214:215], v[112:113] op_sel_hi:[1,0]
	v_pk_mul_f32 v[216:217], v[216:217], v[112:113] op_sel_hi:[1,0]
	v_pk_mul_f32 v[218:219], v[218:219], v[112:113] op_sel_hi:[1,0]
	v_pk_mul_f32 v[220:221], v[220:221], v[112:113] op_sel_hi:[1,0]
	s_waitcnt vmcnt(13)
	v_mov_b32_e32 v115, v110
	v_fma_mix_f32 v116, v110, v70, 0 op_sel_hi:[0,1,0]
	v_fma_mix_f32 v117, v110, v70, 0 op_sel:[0,1,0] op_sel_hi:[0,1,0]
	v_fma_mix_f32 v118, v110, v71, 0 op_sel_hi:[0,1,0]
	v_cvt_pk_fp8_f32 v72, v208, v209
	v_cvt_pk_fp8_f32 v73, v212, v213
	v_cvt_pk_fp8_f32 v74, v216, v217
	v_cvt_pk_fp8_f32 v75, v220, v221
	v_cvt_pk_fp8_f32 v72, v210, v211 op_sel:[0,0,1]
	v_cvt_pk_fp8_f32 v73, v214, v215 op_sel:[0,0,1]
	v_cvt_pk_fp8_f32 v74, v218, v219 op_sel:[0,0,1]
	s_nop 1
	v_mfma_f32_16x16x32_fp8_fp8 v[152:155], v[72:73], v[30:31], 0
	v_mfma_f32_16x16x32_fp8_fp8 v[152:155], v[74:75], v[32:33], v[152:155]
	v_fma_f32 v111, v105, v121, -v123
	v_exp_f32_e32 v111, v111
	s_nop 0
	v_mul_f32_e32 v112, v111, v101
	v_mul_f32_e32 v110, v111, v108
	v_add_f32_e32 v114, v114, v111
	v_pk_mul_f32 v[222:223], v[222:223], v[112:113] op_sel_hi:[1,0]
	v_pk_mul_f32 v[224:225], v[224:225], v[112:113] op_sel_hi:[1,0]
	v_pk_mul_f32 v[226:227], v[226:227], v[112:113] op_sel_hi:[1,0]
	v_pk_mul_f32 v[228:229], v[228:229], v[112:113] op_sel_hi:[1,0]
	v_pk_mul_f32 v[230:231], v[230:231], v[112:113] op_sel_hi:[1,0]
	v_pk_mul_f32 v[232:233], v[232:233], v[112:113] op_sel_hi:[1,0]
	v_pk_mul_f32 v[234:235], v[234:235], v[112:113] op_sel_hi:[1,0]
	s_waitcnt vmcnt(11)
	v_add_f32_e32 v115, v115, v110
	v_fma_mix_f32 v116, v110, v66, v116 op_sel_hi:[0,1,0]
	v_fma_mix_f32 v117, v110, v66, v117 op_sel:[0,1,0] op_sel_hi:[0,1,0]
	v_fma_mix_f32 v118, v110, v67, v118 op_sel_hi:[0,1,0]
	v_cvt_pk_fp8_f32 v76, v222, v223
	v_cvt_pk_fp8_f32 v77, v226, v227
	v_cvt_pk_fp8_f32 v78, v230, v231
	v_cvt_pk_fp8_f32 v79, v234, v235
	v_cvt_pk_fp8_f32 v76, v224, v225 op_sel:[0,0,1]
	v_cvt_pk_fp8_f32 v77, v228, v229 op_sel:[0,0,1]
	v_cvt_pk_fp8_f32 v78, v232, v233 op_sel:[0,0,1]
	s_nop 1
	v_mfma_f32_16x16x32_fp8_fp8 v[152:155], v[76:77], v[26:27], v[152:155]
	v_mfma_f32_16x16x32_fp8_fp8 v[152:155], v[78:79], v[28:29], v[152:155]
	v_fma_f32 v111, v106, v121, -v123
	v_exp_f32_e32 v111, v111
	s_nop 0
	v_mul_f32_e32 v112, v111, v102
	v_mul_f32_e32 v110, v111, v109
	v_add_f32_e32 v114, v114, v111
	v_pk_mul_f32 v[236:237], v[236:237], v[112:113] op_sel_hi:[1,0]
	v_pk_mul_f32 v[238:239], v[238:239], v[112:113] op_sel_hi:[1,0]
	v_pk_mul_f32 v[240:241], v[240:241], v[112:113] op_sel_hi:[1,0]
	v_pk_mul_f32 v[242:243], v[242:243], v[112:113] op_sel_hi:[1,0]
	v_pk_mul_f32 v[244:245], v[244:245], v[112:113] op_sel_hi:[1,0]
	v_pk_mul_f32 v[246:247], v[246:247], v[112:113] op_sel_hi:[1,0]
	v_pk_mul_f32 v[248:249], v[248:249], v[112:113] op_sel_hi:[1,0]
	s_waitcnt vmcnt(9)
	v_add_f32_e32 v115, v115, v110
	v_fma_mix_f32 v116, v110, v68, v116 op_sel_hi:[0,1,0]
	v_fma_mix_f32 v117, v110, v68, v117 op_sel:[0,1,0] op_sel_hi:[0,1,0]
	v_fma_mix_f32 v118, v110, v69, v118 op_sel_hi:[0,1,0]
	v_cvt_pk_fp8_f32 v80, v236, v237
	v_cvt_pk_fp8_f32 v81, v240, v241
	v_cvt_pk_fp8_f32 v82, v244, v245
	v_cvt_pk_fp8_f32 v83, v248, v249
	v_cvt_pk_fp8_f32 v80, v238, v239 op_sel:[0,0,1]
	v_cvt_pk_fp8_f32 v81, v242, v243 op_sel:[0,0,1]
	v_cvt_pk_fp8_f32 v82, v246, v247 op_sel:[0,0,1]
	s_nop 1
	v_mfma_f32_16x16x32_fp8_fp8 v[152:155], v[80:81], v[18:19], v[152:155]
	v_mfma_f32_16x16x32_fp8_fp8 v[152:155], v[82:83], v[20:21], v[152:155]
	v_mov_b32_e32 v86, v114
	v_mov_b32_e32 v87, v115
	v_mov_b32_e32 v88, v116
	v_mov_b32_e32 v89, v117
	v_mov_b32_e32 v90, v118
	v_permlane16_swap_b32_e32 v114, v86
	v_permlane16_swap_b32_e32 v115, v87
	v_permlane16_swap_b32_e32 v116, v88
	v_permlane16_swap_b32_e32 v117, v89
	v_permlane16_swap_b32_e32 v118, v90
	v_add_f32_e32 v114, v114, v86
	v_add_f32_e32 v115, v115, v87
	v_add_f32_e32 v116, v116, v88
	v_add_f32_e32 v117, v117, v89
	v_add_f32_e32 v118, v118, v90
	v_mov_b32_e32 v86, v114
	v_mov_b32_e32 v87, v115
	v_mov_b32_e32 v88, v116
	v_mov_b32_e32 v89, v117
	v_mov_b32_e32 v90, v118
	v_permlane32_swap_b32_e32 v114, v86
	v_permlane32_swap_b32_e32 v115, v87
	v_permlane32_swap_b32_e32 v116, v88
	v_permlane32_swap_b32_e32 v117, v89
	v_permlane32_swap_b32_e32 v118, v90
	v_add_f32_e32 v37, v114, v86
	v_add_f32_e32 v20, v115, v87
	v_add_f32_e32 v18, v116, v88
	v_add_f32_e32 v19, v117, v89
	v_add_f32_e32 v21, v118, v90
	ds_write2_b32 v156, v152, v153 offset0:0 offset1:20
	ds_write2_b32 v156, v154, v155 offset0:40 offset1:60
	s_branch .LBB1_30
